# v75 + one static priority raise (s_setprio 1) for waves 4-7 over the attention phase
# baseline (speedup 1.0000x reference)
; #define LAS __attribute__((address_space(3)))
;     __device__ __forceinline__ int vcu() const { return (G % 8 == 0) ? (c % 8) * (G / 8) + c / 8 : c; }
;     __device__ __forceinline__ int vcu() const { return (G % 8 == 0) ? (c % 8) * (G / 8) + c / 8 : c; }
; __device__ __forceinline__ void ph_attn_fast2(const Args& a, LAS unsigned char* lds) {
;     ...
;     const int vcu = (gridDim.x % 8 == 0) ? (int)((blockIdx.x % 8) * (gridDim.x / 8) + blockIdx.x / 8) : (int)blockIdx.x;
;     int cvt_next = (int)blockIdx.x * 8 + wave; const int cvt_stride = (int)gridDim.x * 8;
;     LAS float* cvt_scr = (LAS float*)(lds + AT2_PS + wave * 8448);
;     int seam = 0;
;     bool cmp_pref = false;
;     for (int pr = vcu; pr < 1024; pr += gridDim.x) {
.LBB0_1917:
	s_cmp_lt_i32 s58, 16
	s_cselect_b64 s[0:1], -1, 0
	s_cmp_gt_i32 s59, 15
	s_cselect_b64 s[2:3], -1, 0
	s_and_b64 s[0:1], s[0:1], s[2:3]
	s_andn2_b64 vcc, exec, s[0:1]
	s_cbranch_vccnz .LBB0_2342
	v_readfirstlane_b32 s32, v0
	s_cmp_lt_u32 s32, 0x100
	s_cbranch_scc1 .Lattn_prio_skip
	s_setprio 1
.Lattn_prio_skip:
	s_load_dword s1, s[82:83], 0x120
	s_add_u32 s4, s82, 0x120
	s_addc_u32 s5, s83, 0
	v_writelane_b32 v252, s4, 9
	v_readfirstlane_b32 s2, v0
	s_waitcnt lgkmcnt(0)
	s_and_b32 s0, s1, 7
	v_writelane_b32 v252, s5, 10
	s_cmp_lg_u32 s0, 0
	s_mov_b32 s4, s33
	v_writelane_b32 v252, s1, 11
	s_cbranch_scc1 .LBB0_1920
	s_load_dword s1, s[82:83], 0x120
	s_and_b32 s0, s33, 7
	s_waitcnt lgkmcnt(0)
	s_lshr_b32 s1, s1, 3
	s_mul_i32 s0, s1, s0
	s_lshr_b32 s1, s33, 3
	s_add_i32 s4, s0, s1
	s_load_dword s1, s[82:83], 0x120

; __device__ __forceinline__ unsigned xb_ld(unsigned* p)              { return __hip_atomic_load(p, __ATOMIC_RELAXED, __HIP_MEMORY_SCOPE_AGENT); }
; __device__ __forceinline__ unsigned xb_add(unsigned* p, unsigned v) { return __hip_atomic_fetch_add(p, v, __ATOMIC_RELAXED, __HIP_MEMORY_SCOPE_AGENT); }
; #define XB_SPIN(cond, bar) do { unsigned _sp = 0; while (cond) { __builtin_amdgcn_s_sleep(1); \
;     if ((++_sp & 255u) == 0u) { if (xb_ld(&(bar)[XB_TMO])) break; if (_sp > XB_SPIN_CAP) { atomicAdd(&(bar)[XB_TMO], 1u); break; } } } } while (0)
; __device__ __forceinline__ void xcd_barrier(const XcdBarrier& b) {
;     asm volatile("s_waitcnt vmcnt(0)" ::: "memory");
;     __syncthreads();
;     if (threadIdx.x == 0) {
;         unsigned* bar = b.bar;
;         __builtin_amdgcn_s_waitcnt(0);
;         unsigned nloc = b.st[0], nx = b.st[1];
;         if (nloc == 0u) { xcd_barrier_complete(bar, b.x, nloc, nx); b.st[0] = nloc; b.st[1] = nx; }
;         const unsigned old = xb_add(&bar[XB_XSUB(b.x)], 1u);
;         const unsigned gen = old / nloc;
;         if (old + 1u == (gen + 1u) * nloc) {
;             __builtin_amdgcn_fence(__ATOMIC_RELEASE, "agent");
;             asm volatile("s_waitcnt vmcnt(0)" ::: "memory");
;             const unsigned og = xb_add(&bar[XB_TOP], 1u);
;             const unsigned tg = og / nx;
;             if (og + 1u == (tg + 1u) * nx) xb_add(&bar[XB_TOPGEN], 1u);
;             else XB_SPIN(xb_ld(&bar[XB_TOPGEN]) == tg, bar);
.LBB0_2288:
	s_setprio 0
	s_cmp_lt_i32 s59, 17
	s_cbranch_scc1 .LBB0_2342
	s_getreg_b32 s4, hwreg(HW_REG_XCC_ID, 0, 4)
	s_waitcnt vmcnt(0)
	s_waitcnt vmcnt(0) lgkmcnt(0)
	s_barrier
	s_mov_b64 s[0:1], exec
	v_readlane_b32 s2, v252, 2
	v_readlane_b32 s3, v252, 3
	s_and_b64 s[2:3], s[0:1], s[2:3]
	s_mov_b64 exec, s[2:3]
	s_cbranch_execz .LBB0_2341
	s_add_i32 s5, 0, 0x27fe0
	v_mov_b32_e32 v1, s5
	s_load_dwordx2 s[2:3], s[82:83], 0xf0
	s_waitcnt vmcnt(0) expcnt(0) lgkmcnt(0)
	ds_read_b32 v3, v1
	s_add_i32 s5, 0, 0x27fe4
	v_mov_b32_e32 v1, s5
	ds_read_b32 v1, v1
	s_and_b32 s33, s4, 15
	s_waitcnt lgkmcnt(1)
	v_cmp_ne_u32_e32 vcc, 0, v3
	s_cbranch_vccnz .LBB0_2305
	v_readlane_b32 s4, v252, 9
	v_readlane_b32 s5, v252, 10
	s_load_dwordx2 s[8:9], s[4:5], 0x4
	s_add_u32 s4, s2, 0x4200
	s_addc_u32 s5, s3, 0
	s_add_u32 s6, s2, 0x4400
	s_addc_u32 s7, s3, 0
	v_readlane_b32 s10, v252, 11
	s_waitcnt lgkmcnt(0)
	s_mul_i32 s46, s8, s10
	s_add_u32 s8, s2, 0x4500
	s_mul_i32 s46, s46, s9
	s_addc_u32 s9, s3, 0
	s_add_u32 s10, s2, 0x4600
	s_addc_u32 s11, s3, 0
	s_add_u32 s12, s2, 0x4700
	s_addc_u32 s13, s3, 0
	s_add_u32 s14, s2, 0x4800
	s_addc_u32 s15, s3, 0
	s_add_u32 s16, s2, 0x4900
	s_addc_u32 s17, s3, 0
	s_add_u32 s18, s2, 0x4a00
	s_addc_u32 s19, s3, 0
	s_add_u32 s20, s2, 0x4b00
	s_addc_u32 s21, s3, 0
	s_add_u32 s22, s2, 0x4c00
	s_addc_u32 s23, s3, 0
	s_add_u32 s24, s2, 0x4d00
	s_addc_u32 s25, s3, 0
	s_add_u32 s26, s2, 0x4e00
	s_addc_u32 s27, s3, 0
	s_add_u32 s28, s2, 0x4f00
	s_addc_u32 s29, s3, 0
	s_add_u32 s30, s2, 0x5000
	s_addc_u32 s31, s3, 0
	s_add_u32 s34, s2, 0x5100
	s_addc_u32 s35, s3, 0
	s_add_u32 s36, s2, 0x5200
	s_addc_u32 s37, s3, 0
	s_add_u32 s38, s2, 0x5300
	s_addc_u32 s39, s3, 0
	s_mov_b32 s47, 1
	v_mov_b32_e32 v17, 0
	s_branch .LBB0_2293
